# down-GEMM epilogue: 8 per-row gate loads issued together and waited once (stores no longer drained each iteration); plus barrier edits of previous version
# speedup vs baseline: 1.0237x; 1.0018x over previous
.LBB0_1184:
	v_lshl_add_u32 v12, s59, 8, v190
	v_ashrrev_i32_e32 v13, 31, v12
	s_nop 15
	s_nop 15
	v_lshl_add_u64 v[0:1], v[12:13], 2, s[10:11]
	global_load_dword v236, v[0:1], off
	global_load_dword v238, v[0:1], off offset:64
	global_load_dword v240, v[0:1], off offset:128
	global_load_dword v242, v[0:1], off offset:192
	global_load_dword v244, v[0:1], off offset:512
	global_load_dword v246, v[0:1], off offset:576
	global_load_dword v248, v[0:1], off offset:640
	global_load_dword v250, v[0:1], off offset:704
	s_waitcnt vmcnt(0)
	s_lshl_b32 s0, s22, 8
	s_and_b32 s0, s0, 0x300
	v_or_b32_e32 v5, s0, v192
	v_lshlrev_b64 v[2:3], 11, v[12:13]
	v_or_b32_e32 v14, 16, v12
	v_lshl_add_u64 v[2:3], s[8:9], 0, v[2:3]
	v_lshlrev_b32_e32 v172, 1, v5
	v_ashrrev_i32_e32 v15, 31, v14
	v_lshl_add_u64 v[2:3], v[2:3], 0, v[172:173]
	v_lshl_add_u64 v[16:17], v[14:15], 2, s[10:11]
	v_pk_mul_f32 v[6:7], v[158:159], v[236:237] op_sel_hi:[1,0]
	v_pk_mul_f32 v[8:9], v[156:157], v[236:237] op_sel_hi:[1,0]
	v_pk_mul_f32 v[10:11], v[154:155], v[236:237] op_sel_hi:[1,0]
	v_pk_mul_f32 v[18:19], v[152:153], v[236:237] op_sel_hi:[1,0]
	v_pk_mul_f32 v[20:21], v[150:151], v[236:237] op_sel_hi:[1,0]
	v_pk_mul_f32 v[22:23], v[148:149], v[236:237] op_sel_hi:[1,0]
	v_pk_mul_f32 v[24:25], v[146:147], v[236:237] op_sel_hi:[1,0]
	v_pk_mul_f32 v[26:27], v[144:145], v[236:237] op_sel_hi:[1,0]
	v_cvt_pk_bf16_f32 v4, v8, v9
	v_cvt_pk_bf16_f32 v5, v6, v7
	v_cvt_pk_bf16_f32 v6, v18, v19
	v_cvt_pk_bf16_f32 v7, v10, v11
	v_cvt_pk_bf16_f32 v8, v22, v23
	v_cvt_pk_bf16_f32 v9, v20, v21
	v_cvt_pk_bf16_f32 v10, v26, v27
	v_cvt_pk_bf16_f32 v11, v24, v25
	global_store_dwordx4 v[2:3], v[4:7], off
	global_store_dwordx4 v[2:3], v[8:11], off offset:256
	s_nop 1
	v_lshlrev_b64 v[6:7], 11, v[14:15]
	v_lshl_add_u64 v[6:7], s[8:9], 0, v[6:7]
	v_or_b32_e32 v16, 32, v12
	v_lshl_add_u64 v[18:19], v[6:7], 0, v[172:173]
	v_ashrrev_i32_e32 v17, 31, v16
	v_lshl_add_u64 v[14:15], v[16:17], 2, s[10:11]
	v_or_b32_e32 v12, 48, v12
	v_ashrrev_i32_e32 v13, 31, v12
	v_pk_mul_f32 v[6:7], v[142:143], v[238:239] op_sel_hi:[1,0]
	v_pk_mul_f32 v[8:9], v[140:141], v[238:239] op_sel_hi:[1,0]
	v_pk_mul_f32 v[10:11], v[138:139], v[238:239] op_sel_hi:[1,0]
	v_pk_mul_f32 v[20:21], v[136:137], v[238:239] op_sel_hi:[1,0]
	v_pk_mul_f32 v[22:23], v[134:135], v[238:239] op_sel_hi:[1,0]
	v_pk_mul_f32 v[24:25], v[132:133], v[238:239] op_sel_hi:[1,0]
	v_pk_mul_f32 v[26:27], v[130:131], v[238:239] op_sel_hi:[1,0]
	v_pk_mul_f32 v[28:29], v[128:129], v[238:239] op_sel_hi:[1,0]
	v_cvt_pk_bf16_f32 v4, v8, v9
	v_cvt_pk_bf16_f32 v5, v6, v7
	v_cvt_pk_bf16_f32 v6, v20, v21
	v_cvt_pk_bf16_f32 v7, v10, v11
	v_cvt_pk_bf16_f32 v8, v24, v25
	v_cvt_pk_bf16_f32 v9, v22, v23
	v_cvt_pk_bf16_f32 v10, v28, v29
	v_cvt_pk_bf16_f32 v11, v26, v27
	global_store_dwordx4 v[18:19], v[4:7], off
	global_store_dwordx4 v[18:19], v[8:11], off offset:256
	s_nop 1
	v_lshlrev_b64 v[6:7], 11, v[16:17]
	v_lshl_add_u64 v[6:7], s[8:9], 0, v[6:7]
	v_lshl_add_u64 v[16:17], v[6:7], 0, v[172:173]
	v_lshl_add_u64 v[14:15], v[12:13], 2, s[10:11]
	v_pk_mul_f32 v[6:7], v[126:127], v[240:241] op_sel_hi:[1,0]
	v_pk_mul_f32 v[8:9], v[124:125], v[240:241] op_sel_hi:[1,0]
	v_pk_mul_f32 v[10:11], v[122:123], v[240:241] op_sel_hi:[1,0]
	v_pk_mul_f32 v[18:19], v[120:121], v[240:241] op_sel_hi:[1,0]
	v_pk_mul_f32 v[20:21], v[118:119], v[240:241] op_sel_hi:[1,0]
	v_pk_mul_f32 v[22:23], v[116:117], v[240:241] op_sel_hi:[1,0]
	v_pk_mul_f32 v[24:25], v[114:115], v[240:241] op_sel_hi:[1,0]
	v_pk_mul_f32 v[26:27], v[112:113], v[240:241] op_sel_hi:[1,0]
	v_cvt_pk_bf16_f32 v4, v8, v9
	v_cvt_pk_bf16_f32 v5, v6, v7
	v_cvt_pk_bf16_f32 v6, v18, v19
	v_cvt_pk_bf16_f32 v7, v10, v11
	v_cvt_pk_bf16_f32 v8, v22, v23
	v_cvt_pk_bf16_f32 v9, v20, v21
	v_cvt_pk_bf16_f32 v10, v26, v27
	v_cvt_pk_bf16_f32 v11, v24, v25
	global_store_dwordx4 v[16:17], v[4:7], off
	global_store_dwordx4 v[16:17], v[8:11], off offset:256
	s_nop 1
	v_lshlrev_b64 v[6:7], 11, v[12:13]
	v_lshl_add_u64 v[6:7], s[8:9], 0, v[6:7]
	v_lshl_add_u64 v[12:13], v[6:7], 0, v[172:173]
	v_pk_mul_f32 v[6:7], v[110:111], v[242:243] op_sel_hi:[1,0]
	v_pk_mul_f32 v[8:9], v[108:109], v[242:243] op_sel_hi:[1,0]
	v_pk_mul_f32 v[10:11], v[106:107], v[242:243] op_sel_hi:[1,0]
	v_pk_mul_f32 v[14:15], v[104:105], v[242:243] op_sel_hi:[1,0]
	v_pk_mul_f32 v[16:17], v[102:103], v[242:243] op_sel_hi:[1,0]
	v_pk_mul_f32 v[18:19], v[100:101], v[242:243] op_sel_hi:[1,0]
	v_pk_mul_f32 v[20:21], v[98:99], v[242:243] op_sel_hi:[1,0]
	v_pk_mul_f32 v[22:23], v[96:97], v[242:243] op_sel_hi:[1,0]
	v_cvt_pk_bf16_f32 v4, v8, v9
	v_cvt_pk_bf16_f32 v5, v6, v7
	v_cvt_pk_bf16_f32 v6, v14, v15
	v_cvt_pk_bf16_f32 v7, v10, v11
	v_cvt_pk_bf16_f32 v8, v18, v19
	v_cvt_pk_bf16_f32 v9, v16, v17
	v_cvt_pk_bf16_f32 v10, v22, v23
	v_cvt_pk_bf16_f32 v11, v20, v21
	global_store_dwordx4 v[12:13], v[4:7], off
	global_store_dwordx4 v[12:13], v[8:11], off offset:256
	s_nop 1
	v_add_co_u32_e32 v14, vcc, s47, v2
	v_lshl_add_u64 v[12:13], v[2:3], 0, s[16:17]
	s_nop 0
	v_addc_co_u32_e32 v15, vcc, 0, v3, vcc
	v_pk_mul_f32 v[6:7], v[94:95], v[244:245] op_sel_hi:[1,0]
	v_pk_mul_f32 v[8:9], v[92:93], v[244:245] op_sel_hi:[1,0]
	v_pk_mul_f32 v[10:11], v[90:91], v[244:245] op_sel_hi:[1,0]
	v_pk_mul_f32 v[16:17], v[88:89], v[244:245] op_sel_hi:[1,0]
	v_pk_mul_f32 v[18:19], v[86:87], v[244:245] op_sel_hi:[1,0]
	v_pk_mul_f32 v[20:21], v[84:85], v[244:245] op_sel_hi:[1,0]
	v_pk_mul_f32 v[22:23], v[82:83], v[244:245] op_sel_hi:[1,0]
	v_pk_mul_f32 v[24:25], v[80:81], v[244:245] op_sel_hi:[1,0]
	v_cvt_pk_bf16_f32 v4, v8, v9
	v_cvt_pk_bf16_f32 v5, v6, v7
	v_cvt_pk_bf16_f32 v6, v16, v17
	v_cvt_pk_bf16_f32 v7, v10, v11
	v_cvt_pk_bf16_f32 v8, v20, v21
	v_cvt_pk_bf16_f32 v9, v18, v19
	v_cvt_pk_bf16_f32 v10, v24, v25
	v_cvt_pk_bf16_f32 v11, v22, v23
	global_store_dwordx4 v[14:15], v[4:7], off
	global_store_dwordx4 v[12:13], v[8:11], off offset:256
	s_nop 1
	v_add_co_u32_e32 v14, vcc, s48, v2
	v_lshl_add_u64 v[12:13], v[2:3], 0, s[18:19]
	s_nop 0
	v_addc_co_u32_e32 v15, vcc, 0, v3, vcc
	v_pk_mul_f32 v[6:7], v[78:79], v[246:247] op_sel_hi:[1,0]
	v_pk_mul_f32 v[8:9], v[76:77], v[246:247] op_sel_hi:[1,0]
	v_pk_mul_f32 v[10:11], v[74:75], v[246:247] op_sel_hi:[1,0]
	v_pk_mul_f32 v[16:17], v[72:73], v[246:247] op_sel_hi:[1,0]
	v_pk_mul_f32 v[18:19], v[70:71], v[246:247] op_sel_hi:[1,0]
	v_pk_mul_f32 v[20:21], v[68:69], v[246:247] op_sel_hi:[1,0]
	v_pk_mul_f32 v[22:23], v[66:67], v[246:247] op_sel_hi:[1,0]
	v_pk_mul_f32 v[24:25], v[64:65], v[246:247] op_sel_hi:[1,0]
	v_cvt_pk_bf16_f32 v4, v8, v9
	v_cvt_pk_bf16_f32 v5, v6, v7
	v_cvt_pk_bf16_f32 v6, v16, v17
	v_cvt_pk_bf16_f32 v7, v10, v11
	v_cvt_pk_bf16_f32 v8, v20, v21
	v_cvt_pk_bf16_f32 v9, v18, v19
	v_cvt_pk_bf16_f32 v10, v24, v25
	v_cvt_pk_bf16_f32 v11, v22, v23
	global_store_dwordx4 v[14:15], v[4:7], off
	global_store_dwordx4 v[12:13], v[8:11], off offset:256
	s_nop 1
	v_add_co_u32_e32 v14, vcc, s49, v2
	v_lshl_add_u64 v[12:13], v[2:3], 0, s[20:21]
	s_nop 0
	v_addc_co_u32_e32 v15, vcc, 0, v3, vcc
	s_and_b64 vcc, exec, s[6:7]
	v_pk_mul_f32 v[6:7], v[62:63], v[248:249] op_sel_hi:[1,0]
	v_pk_mul_f32 v[8:9], v[60:61], v[248:249] op_sel_hi:[1,0]
	v_pk_mul_f32 v[10:11], v[58:59], v[248:249] op_sel_hi:[1,0]
	v_pk_mul_f32 v[16:17], v[56:57], v[248:249] op_sel_hi:[1,0]
	v_pk_mul_f32 v[18:19], v[54:55], v[248:249] op_sel_hi:[1,0]
	v_pk_mul_f32 v[20:21], v[52:53], v[248:249] op_sel_hi:[1,0]
	v_pk_mul_f32 v[22:23], v[50:51], v[248:249] op_sel_hi:[1,0]
	v_pk_mul_f32 v[24:25], v[48:49], v[248:249] op_sel_hi:[1,0]
	v_cvt_pk_bf16_f32 v4, v8, v9
	v_cvt_pk_bf16_f32 v5, v6, v7
	v_cvt_pk_bf16_f32 v6, v16, v17
	v_cvt_pk_bf16_f32 v7, v10, v11
	v_cvt_pk_bf16_f32 v8, v20, v21
	v_cvt_pk_bf16_f32 v9, v18, v19
	v_cvt_pk_bf16_f32 v10, v24, v25
	v_cvt_pk_bf16_f32 v11, v22, v23
	global_store_dwordx4 v[14:15], v[4:7], off
	global_store_dwordx4 v[12:13], v[8:11], off offset:256
	s_nop 1
	v_pk_mul_f32 v[4:5], v[44:45], v[250:251] op_sel_hi:[1,0]
	v_add_co_u32_e64 v10, s[0:1], s43, v2
	v_lshl_add_u64 v[8:9], v[2:3], 0, s[2:3]
	s_nop 0
	v_addc_co_u32_e64 v11, s[0:1], 0, v3, s[0:1]
	v_pk_mul_f32 v[2:3], v[46:47], v[250:251] op_sel_hi:[1,0]
	v_pk_mul_f32 v[6:7], v[42:43], v[250:251] op_sel_hi:[1,0]
	v_pk_mul_f32 v[12:13], v[40:41], v[250:251] op_sel_hi:[1,0]
	v_pk_mul_f32 v[14:15], v[38:39], v[250:251] op_sel_hi:[1,0]
	v_pk_mul_f32 v[16:17], v[36:37], v[250:251] op_sel_hi:[1,0]
	v_pk_mul_f32 v[18:19], v[34:35], v[250:251] op_sel_hi:[1,0]
	v_pk_mul_f32 v[20:21], v[32:33], v[250:251] op_sel_hi:[1,0]
	v_cvt_pk_bf16_f32 v0, v4, v5
	v_cvt_pk_bf16_f32 v1, v2, v3
	v_cvt_pk_bf16_f32 v2, v12, v13
	v_cvt_pk_bf16_f32 v3, v6, v7
	s_mov_b64 s[0:1], -1
	v_cvt_pk_bf16_f32 v4, v16, v17
	v_cvt_pk_bf16_f32 v5, v14, v15
	v_cvt_pk_bf16_f32 v6, v20, v21
	v_cvt_pk_bf16_f32 v7, v18, v19
	global_store_dwordx4 v[10:11], v[0:3], off
	global_store_dwordx4 v[8:9], v[4:7], off offset:256
	s_nop 1
	s_cbranch_vccnz .LBB0_1173
	s_andn2_b64 vcc, exec, s[4:5]
	s_cbranch_vccnz .LBB0_1172
	s_barrier
	s_branch .LBB0_1172

	.amdhsa_kernel _Z4mega6Params
		.amdhsa_group_segment_fixed_size 0
		.amdhsa_private_segment_fixed_size 0
		.amdhsa_kernarg_size 416
		.amdhsa_user_sgpr_count 2
		.amdhsa_user_sgpr_dispatch_ptr 0
		.amdhsa_user_sgpr_queue_ptr 0
		.amdhsa_user_sgpr_kernarg_segment_ptr 1
		.amdhsa_user_sgpr_dispatch_id 0
		.amdhsa_user_sgpr_kernarg_preload_length 0
		.amdhsa_user_sgpr_kernarg_preload_offset 0
		.amdhsa_user_sgpr_private_segment_size 0
		.amdhsa_uses_dynamic_stack 0
		.amdhsa_enable_private_segment 0
		.amdhsa_system_sgpr_workgroup_id_x 1
		.amdhsa_system_sgpr_workgroup_id_y 0
		.amdhsa_system_sgpr_workgroup_id_z 0
		.amdhsa_system_sgpr_workgroup_info 0
		.amdhsa_system_vgpr_workitem_id 2
		.amdhsa_next_free_vgpr 256
		.amdhsa_next_free_sgpr 102
		.amdhsa_accum_offset 256
		.amdhsa_reserve_vcc 1
		.amdhsa_float_round_mode_32 0
		.amdhsa_float_round_mode_16_64 0
		.amdhsa_float_denorm_mode_32 3
		.amdhsa_float_denorm_mode_16_64 3
		.amdhsa_dx10_clamp 1
		.amdhsa_ieee_mode 1
		.amdhsa_fp16_overflow 0
		.amdhsa_tg_split 0
		.amdhsa_exception_fp_ieee_invalid_op 0
		.amdhsa_exception_fp_denorm_src 0
		.amdhsa_exception_fp_ieee_div_zero 0
		.amdhsa_exception_fp_ieee_overflow 0
		.amdhsa_exception_fp_ieee_underflow 0
		.amdhsa_exception_fp_ieee_inexact 0
		.amdhsa_exception_int_div_zero 0
	.end_amdhsa_kernel

amdhsa.kernels:
  - .agpr_count:     0
    .args:
      - .offset:         0
        .size:           160
        .value_kind:     by_value
      - .offset:         160
        .size:           4
        .value_kind:     hidden_block_count_x
      - .offset:         164
        .size:           4
        .value_kind:     hidden_block_count_y
      - .offset:         168
        .size:           4
        .value_kind:     hidden_block_count_z
      - .offset:         172
        .size:           2
        .value_kind:     hidden_group_size_x
      - .offset:         174
        .size:           2
        .value_kind:     hidden_group_size_y
      - .offset:         176
        .size:           2
        .value_kind:     hidden_group_size_z
      - .offset:         178
        .size:           2
        .value_kind:     hidden_remainder_x
      - .offset:         180
        .size:           2
        .value_kind:     hidden_remainder_y
      - .offset:         182
        .size:           2
        .value_kind:     hidden_remainder_z
      - .offset:         200
        .size:           8
        .value_kind:     hidden_global_offset_x
      - .offset:         208
        .size:           8
        .value_kind:     hidden_global_offset_y
      - .offset:         216
        .size:           8
        .value_kind:     hidden_global_offset_z
      - .offset:         224
        .size:           2
        .value_kind:     hidden_grid_dims
      - .offset:         248
        .size:           8
        .value_kind:     hidden_multigrid_sync_arg
      - .offset:         280
        .size:           4
        .value_kind:     hidden_dynamic_lds_size
    .group_segment_fixed_size: 0
    .kernarg_segment_align: 8
    .kernarg_segment_size: 416
    .language:       OpenCL C
    .language_version:
      - 2
      - 0
    .max_flat_workgroup_size: 512
    .name:           _Z4mega6Params
    .private_segment_fixed_size: 0
    .sgpr_count:     108
    .sgpr_spill_count: 48
    .symbol:         _Z4mega6Params.kd
    .uniform_work_group_size: 1
    .uses_dynamic_stack: false
    .vgpr_count:     256
    .vgpr_spill_count: 0
    .wavefront_size: 64
